# final candidate + loop back-edge bookkeeping (tile counters, pointer adds, exit test) moved in front of the loop-back barrier in both attention loops
# baseline (speedup 1.0000x reference)
; #define PK4(P, BASE, OUT) do { u32x4 w = {cvtpk(P[BASE + 0], P[BASE + 1]), cvtpk(P[BASE + 2], P[BASE + 3]), cvtpk(P[BASE + 4], P[BASE + 5]), cvtpk(P[BASE + 6], P[BASE + 7])}; \
;     OUT = *reinterpret_cast<bf16x8*>(&w); } while (0)
; __device__ __forceinline__ void smax_tile(f32x16& p0, f32x16& p1, float& mhat, float& l_reg, f32x16 (&o)[4], float* al_l, const bool first, int r32, int hi,
;                                           bf16x8& pa0, bf16x8& pa1, bf16x8& pa2, bf16x8& pa3) {
;     ...
; #pragma unroll
;     for (int r = 0; r < 16; ++r) p0[r] = __builtin_amdgcn_exp2f(p0[r]);
; #pragma unroll
;     for (int r = 0; r < 16; ++r) p1[r] = __builtin_amdgcn_exp2f(p1[r]);
;     float ps = p0[0];
; #pragma unroll
;     for (int r = 1; r < 16; ++r) ps += p0[r];
; #pragma unroll
;     for (int r = 0; r < 16; ++r) ps += p1[r];
;     { auto rr = __builtin_amdgcn_permlane32_swap(__float_as_uint(ps), __float_as_uint(ps), false, false); ps = __uint_as_float(rr[0]) + __uint_as_float(rr[1]); }
;     l_reg += ps;
;     ...
;     PK4(p0, 0, pa0); PK4(p0, 8, pa1); PK4(p1, 0, pa2); PK4(p1, 8, pa3);
.LBB0_605:
	v_exp_f32_e32 v96, v96
	v_exp_f32_e32 v97, v97
	v_exp_f32_e32 v98, v98
	v_exp_f32_e32 v99, v99
	v_exp_f32_e32 v100, v100
	v_exp_f32_e32 v101, v101
	v_add_f32_e32 v160, v96, v97
	v_exp_f32_e32 v102, v102
	v_add_f32_e32 v160, v98, v160
	v_exp_f32_e32 v103, v103
	v_add_f32_e32 v160, v99, v160
	v_exp_f32_e32 v104, v104
	v_add_f32_e32 v160, v100, v160
	v_exp_f32_e32 v105, v105
	v_add_f32_e32 v160, v101, v160
	v_exp_f32_e32 v106, v106
	v_add_f32_e32 v160, v102, v160
	v_exp_f32_e32 v107, v107
	v_add_f32_e32 v160, v103, v160
	v_exp_f32_e32 v108, v108
	v_add_f32_e32 v160, v104, v160
	v_exp_f32_e32 v109, v109
	v_add_f32_e32 v160, v105, v160
	v_exp_f32_e32 v110, v110
	v_add_f32_e32 v160, v106, v160
	v_exp_f32_e32 v111, v111
	v_add_f32_e32 v160, v107, v160
	v_exp_f32_e32 v80, v80
	v_add_f32_e32 v160, v108, v160
	v_exp_f32_e32 v81, v81
	v_add_f32_e32 v160, v109, v160
	v_exp_f32_e32 v82, v82
	v_add_f32_e32 v160, v110, v160
	v_exp_f32_e32 v83, v83
	v_add_f32_e32 v160, v111, v160
	v_exp_f32_e32 v84, v84
	v_add_f32_e32 v160, v80, v160
	v_exp_f32_e32 v85, v85
	v_add_f32_e32 v160, v81, v160
	v_exp_f32_e32 v86, v86
	v_add_f32_e32 v160, v82, v160
	v_exp_f32_e32 v87, v87
	v_add_f32_e32 v160, v83, v160
	v_exp_f32_e32 v88, v88
	v_add_f32_e32 v160, v84, v160
	v_exp_f32_e32 v89, v89
	v_add_f32_e32 v160, v85, v160
	v_exp_f32_e32 v90, v90
	v_add_f32_e32 v160, v86, v160
	v_exp_f32_e32 v91, v91
	v_add_f32_e32 v160, v87, v160
	v_exp_f32_e32 v92, v92
	v_add_f32_e32 v160, v88, v160
	v_exp_f32_e32 v93, v93
	v_add_f32_e32 v160, v89, v160
	v_exp_f32_e32 v94, v94
	v_add_f32_e32 v160, v90, v160
	v_exp_f32_e32 v95, v95
	v_add_f32_e32 v160, v91, v160
	v_add_f32_e32 v160, v92, v160
	v_add_f32_e32 v160, v93, v160
	v_add_f32_e32 v160, v94, v160
	v_add_f32_e32 v160, v95, v160
	v_mov_b32_e32 v161, v160
	v_cvt_pk_bf16_f32 v172, v96, v97
	v_cvt_pk_bf16_f32 v173, v98, v99
	v_permlane32_swap_b32_e32 v160, v161
	v_add_f32_e32 v160, v160, v161
	v_add_f32_e32 v204, v204, v160
	v_cvt_pk_bf16_f32 v174, v100, v101
	v_cvt_pk_bf16_f32 v175, v102, v103
	v_cvt_pk_bf16_f32 v168, v104, v105
	v_cvt_pk_bf16_f32 v169, v106, v107
	v_cvt_pk_bf16_f32 v170, v108, v109
	v_cvt_pk_bf16_f32 v171, v110, v111
	v_cvt_pk_bf16_f32 v164, v80, v81
	v_cvt_pk_bf16_f32 v165, v82, v83
	v_cvt_pk_bf16_f32 v166, v84, v85
	v_cvt_pk_bf16_f32 v167, v86, v87
	v_cvt_pk_bf16_f32 v160, v88, v89
	v_cvt_pk_bf16_f32 v161, v90, v91
	v_cvt_pk_bf16_f32 v162, v92, v93
	v_cvt_pk_bf16_f32 v163, v94, v95
	s_mul_i32 s47, s26, 0x6000
	s_addk_i32 s93, 0xc000
	s_cmp_lg_u32 s26, 0
	s_cselect_b32 s46, s93, 0x8000
	v_add_u32_e32 v227, s46, v202
	v_add_u32_e32 v207, s47, v185
	v_add_u32_e32 v224, s47, v187
	v_add_u32_e32 v225, s47, v205
	v_add_u32_e32 v226, s47, v206
	s_waitcnt lgkmcnt(0)
	ds_read_b64_tr_b16 v[208:209], v227 offset:0
	ds_read_b64_tr_b16 v[210:211], v227 offset:2048
	ds_read_b64_tr_b16 v[212:213], v227 offset:512
	ds_read_b64_tr_b16 v[214:215], v227 offset:2560
	ds_read_b64_tr_b16 v[216:217], v227 offset:1024
	ds_read_b64_tr_b16 v[218:219], v227 offset:3072
	ds_read_b64_tr_b16 v[220:221], v227 offset:1536
	ds_read_b64_tr_b16 v[222:223], v227 offset:3584
	s_barrier
; template <int DQK, bool HASQK, bool HASPV, int J>
; __device__ __forceinline__ void slot_read(bf16x8 (&kf)[DQK / 16][2], s16x4 (&vf)[4][8], const int (&ka_)[4], int vb_) {
;     constexpr int NQS = HASQK ? 2 * (DQK / 16) : 0, NS = NQS + (HASPV ? 16 : 0);
;     if constexpr (J < NQS) { constexpr int d0 = J >> 1, h = J & 1; dsr128<(d0 >> 2) * 128 + h * 32 * DQK * 2>(kf[d0][h], ka_[d0 & 3]); }
;     else if constexpr (J < NS) { constexpr int q = J - NQS, g = q >> 2, d = q & 3; dstr64<v_rd_off(d, g, 0)>(vf[g][2 * d], vb_); dstr64<v_rd_off(d, g, 1)>(vf[g][2 * d + 1], vb_); }
; }
; template <int DQK, bool HASQK, bool HASPV, int J> ...
;     constexpr int NQS = HASQK ? 2 * (DQK / 16) : 0, NS = NQS + (HASPV ? 16 : 0);
;     if constexpr (J < NS) {
;         constexpr int rd1 = (J + 1 < NS) ? ((J + 1 < NQS) ? 1 : 2) : 0, rd2 = (J + 2 < NS) ? ((J + 2 < NQS) ? 1 : 2) : 0, rd3 = (J + 3 < NS) ? ((J + 3 < NQS) ? 1 : 2) : 0, NW = rd1 + rd2 + rd3;
;     ...
;         if constexpr (J < NQS) { constexpr int d0 = J >> 1, h = J & 1;
;             LWN1(kf[d0][h]); SBAR();
;             if constexpr (h == 0) p0 = __builtin_amdgcn_mfma_f32_32x32x16_bf16(kf[d0][0], qr[d0], (d0 == 0) ? negm : p0, 0, 0, 0);
;             else p1 = __builtin_amdgcn_mfma_f32_32x32x16_bf16(kf[d0][1], qr[d0], (d0 == 0) ? negm : p1, 0, 0, 0);
;         } else { constexpr int q = J - NQS, g = q >> 2, d = q & 3;
;             LWN2(vf[g][2 * d], vf[g][2 * d + 1]); SBAR();
;             o[d] = __builtin_amdgcn_mfma_f32_32x32x16_bf16(pa[g], (bf16x8){vf[g][2 * d][0], vf[g][2 * d][1], vf[g][2 * d][2], vf[g][2 * d][3], vf[g][2 * d + 1][0], vf[g][2 * d + 1][1], vf[g][2 * d + 1][2], vf[g][2 * d + 1][3]}, o[d], 0, 0, 0);
;         }
;     ...
;         SBAR();
;         slot_read<DQK, HASQK, HASPV, J + 4>(kf, vf, ka_, vb_);
;         SBAR();
;         slot_run<DQK, HASQK, HASPV, J + 1>(kf, vf, ka_, vb_, qr, p0, p1, negm, o, pa);
;     }
; }
;     ...
;     for (int i = 0; i < NT - 1; ++i) {
;         SEG_S(i);
;         { const int cp = (ci == 0) ? 2 : ci - 1, cn = (ci == 2) ? 0 : ci + 1;
;           if (DMA_M) { if (i + 3 < NT) DMA_K(i + 3, cp); if (i + 2 < NT) DMA_V(i + 2, cn); }
;           SEG_M(true, true, ci, cp);
;           if (DMA_M && i + 3 < NT) asm volatile("s_waitcnt vmcnt(%0)" :: "n"(NKW + 2) : "memory");
;           else asm volatile("s_waitcnt vmcnt(0)" ::: "memory");
;           BAR_ALL(); }
	s_waitcnt lgkmcnt(6)
	v_mfma_f32_32x32x16_bf16 v[64:79], v[172:175], v[208:211], v[64:79]
	ds_read_b64_tr_b16 v[208:209], v227 offset:4096
	ds_read_b64_tr_b16 v[210:211], v227 offset:6144
	s_waitcnt lgkmcnt(6)
	v_mfma_f32_32x32x16_bf16 v[48:63], v[172:175], v[212:215], v[48:63]
	ds_read_b64_tr_b16 v[212:213], v227 offset:4608
	ds_read_b64_tr_b16 v[214:215], v227 offset:6656
	s_waitcnt lgkmcnt(6)
	v_mfma_f32_32x32x16_bf16 v[32:47], v[172:175], v[216:219], v[32:47]
	ds_read_b64_tr_b16 v[216:217], v227 offset:5120
	ds_read_b64_tr_b16 v[218:219], v227 offset:7168
	s_waitcnt lgkmcnt(6)
	v_mfma_f32_32x32x16_bf16 v[16:31], v[172:175], v[220:223], v[16:31]
	ds_read_b64_tr_b16 v[220:221], v227 offset:5632
	ds_read_b64_tr_b16 v[222:223], v227 offset:7680
	s_waitcnt lgkmcnt(6)
	v_mfma_f32_32x32x16_bf16 v[64:79], v[168:171], v[208:211], v[64:79]
	ds_read_b64_tr_b16 v[208:209], v227 offset:8192
	ds_read_b64_tr_b16 v[210:211], v227 offset:10240
	s_waitcnt lgkmcnt(6)
	v_mfma_f32_32x32x16_bf16 v[48:63], v[168:171], v[212:215], v[48:63]
	ds_read_b64_tr_b16 v[212:213], v227 offset:8704
	ds_read_b64_tr_b16 v[214:215], v227 offset:10752
	s_waitcnt lgkmcnt(6)
	v_mfma_f32_32x32x16_bf16 v[32:47], v[168:171], v[216:219], v[32:47]
	ds_read_b64_tr_b16 v[216:217], v227 offset:9216
	ds_read_b64_tr_b16 v[218:219], v227 offset:11264
	s_waitcnt lgkmcnt(6)
	v_mfma_f32_32x32x16_bf16 v[16:31], v[168:171], v[220:223], v[16:31]
	ds_read_b64_tr_b16 v[220:221], v227 offset:9728
	ds_read_b64_tr_b16 v[222:223], v227 offset:11776
	s_waitcnt lgkmcnt(6)
	v_mfma_f32_32x32x16_bf16 v[64:79], v[164:167], v[208:211], v[64:79]
	ds_read_b64_tr_b16 v[208:209], v227 offset:12288
	ds_read_b64_tr_b16 v[210:211], v227 offset:14336
	s_waitcnt lgkmcnt(6)
	v_mfma_f32_32x32x16_bf16 v[48:63], v[164:167], v[212:215], v[48:63]
	ds_read_b64_tr_b16 v[212:213], v227 offset:12800
	ds_read_b64_tr_b16 v[214:215], v227 offset:14848
	s_waitcnt lgkmcnt(6)
	v_mfma_f32_32x32x16_bf16 v[32:47], v[164:167], v[216:219], v[32:47]
	ds_read_b64_tr_b16 v[216:217], v227 offset:13312
	ds_read_b64_tr_b16 v[218:219], v227 offset:15360
	s_waitcnt lgkmcnt(6)
	v_mfma_f32_32x32x16_bf16 v[16:31], v[164:167], v[220:223], v[16:31]
	ds_read_b64_tr_b16 v[220:221], v227 offset:13824
	ds_read_b64_tr_b16 v[222:223], v227 offset:15872
	v_xor_b32_e32 v80, 0x80000000, v203
	v_mov_b32_e32 v81, v80
	v_mov_b32_e32 v82, v80
	v_mov_b32_e32 v83, v80
	v_mov_b32_e32 v84, v80
	v_mov_b32_e32 v85, v80
	v_mov_b32_e32 v86, v80
	v_mov_b32_e32 v87, v80
	v_mov_b32_e32 v88, v80
	v_mov_b32_e32 v89, v80
	v_mov_b32_e32 v90, v80
	v_mov_b32_e32 v91, v80
	v_mov_b32_e32 v92, v80
	v_mov_b32_e32 v93, v80
	v_mov_b32_e32 v94, v80
	v_mov_b32_e32 v95, v80
	s_waitcnt lgkmcnt(6)
	v_mfma_f32_32x32x16_bf16 v[64:79], v[160:163], v[208:211], v[64:79]
	ds_read_b128 v[208:211], v207 offset:0
	s_waitcnt lgkmcnt(5)
	v_mfma_f32_32x32x16_bf16 v[48:63], v[160:163], v[212:215], v[48:63]
	ds_read_b128 v[212:215], v207 offset:12288
	s_waitcnt lgkmcnt(4)
	v_mfma_f32_32x32x16_bf16 v[32:47], v[160:163], v[216:219], v[32:47]
	ds_read_b128 v[216:219], v224 offset:0
	s_waitcnt lgkmcnt(3)
	v_mfma_f32_32x32x16_bf16 v[16:31], v[160:163], v[220:223], v[16:31]
	ds_read_b128 v[220:223], v224 offset:12288
	s_waitcnt lgkmcnt(3)
	v_mfma_f32_32x32x16_bf16 v[96:111], v[208:211], v[112:115], v[80:95]
	ds_read_b128 v[208:211], v225 offset:0
	s_waitcnt lgkmcnt(3)
	v_mfma_f32_32x32x16_bf16 v[80:95], v[212:215], v[112:115], v[80:95]
	ds_read_b128 v[212:215], v225 offset:12288
	s_waitcnt lgkmcnt(3)
	v_mfma_f32_32x32x16_bf16 v[96:111], v[216:219], v[116:119], v[96:111]
	ds_read_b128 v[216:219], v226 offset:0
	s_waitcnt lgkmcnt(3)
	v_mfma_f32_32x32x16_bf16 v[80:95], v[220:223], v[116:119], v[80:95]
	ds_read_b128 v[220:223], v226 offset:12288
	s_waitcnt lgkmcnt(3)
	v_mfma_f32_32x32x16_bf16 v[96:111], v[208:211], v[120:123], v[96:111]
	ds_read_b128 v[208:211], v207 offset:128
	s_waitcnt lgkmcnt(3)
	v_mfma_f32_32x32x16_bf16 v[80:95], v[212:215], v[120:123], v[80:95]
	ds_read_b128 v[212:215], v207 offset:12416
	s_waitcnt lgkmcnt(3)
	v_mfma_f32_32x32x16_bf16 v[96:111], v[216:219], v[124:127], v[96:111]
	ds_read_b128 v[216:219], v224 offset:128
	s_waitcnt lgkmcnt(3)
	v_mfma_f32_32x32x16_bf16 v[80:95], v[220:223], v[124:127], v[80:95]
	ds_read_b128 v[220:223], v224 offset:12416
	s_waitcnt lgkmcnt(3)
	v_mfma_f32_32x32x16_bf16 v[96:111], v[208:211], v[128:131], v[96:111]
	ds_read_b128 v[208:211], v225 offset:128
	s_waitcnt lgkmcnt(3)
	v_mfma_f32_32x32x16_bf16 v[80:95], v[212:215], v[128:131], v[80:95]
	ds_read_b128 v[212:215], v225 offset:12416
	s_waitcnt lgkmcnt(3)
	v_mfma_f32_32x32x16_bf16 v[96:111], v[216:219], v[132:135], v[96:111]
	ds_read_b128 v[216:219], v226 offset:128
	s_waitcnt lgkmcnt(3)
	v_mfma_f32_32x32x16_bf16 v[80:95], v[220:223], v[132:135], v[80:95]
	ds_read_b128 v[220:223], v226 offset:12416
	s_waitcnt lgkmcnt(3)
	v_mfma_f32_32x32x16_bf16 v[96:111], v[208:211], v[136:139], v[96:111]
	ds_read_b128 v[208:211], v207 offset:256
	s_waitcnt lgkmcnt(3)
	v_mfma_f32_32x32x16_bf16 v[80:95], v[212:215], v[136:139], v[80:95]
	ds_read_b128 v[212:215], v207 offset:12544
	s_waitcnt lgkmcnt(3)
	v_mfma_f32_32x32x16_bf16 v[96:111], v[216:219], v[140:143], v[96:111]
	ds_read_b128 v[216:219], v224 offset:256
	s_waitcnt lgkmcnt(3)
	v_mfma_f32_32x32x16_bf16 v[80:95], v[220:223], v[140:143], v[80:95]
	ds_read_b128 v[220:223], v224 offset:12544
	s_waitcnt lgkmcnt(3)
	v_mfma_f32_32x32x16_bf16 v[96:111], v[208:211], v[144:147], v[96:111]
	ds_read_b128 v[208:211], v225 offset:256
	s_waitcnt lgkmcnt(3)
	v_mfma_f32_32x32x16_bf16 v[80:95], v[212:215], v[144:147], v[80:95]
	ds_read_b128 v[212:215], v225 offset:12544
	s_waitcnt lgkmcnt(3)
	v_mfma_f32_32x32x16_bf16 v[96:111], v[216:219], v[148:151], v[96:111]
	ds_read_b128 v[216:219], v226 offset:256
	s_waitcnt lgkmcnt(3)
	v_mfma_f32_32x32x16_bf16 v[80:95], v[220:223], v[148:151], v[80:95]
	ds_read_b128 v[220:223], v226 offset:12544
	s_waitcnt lgkmcnt(3)
	v_mfma_f32_32x32x16_bf16 v[96:111], v[208:211], v[152:155], v[96:111]
	s_waitcnt lgkmcnt(2)
	v_mfma_f32_32x32x16_bf16 v[80:95], v[212:215], v[152:155], v[80:95]
	s_waitcnt lgkmcnt(1)
	v_mfma_f32_32x32x16_bf16 v[96:111], v[216:219], v[156:159], v[96:111]
	s_waitcnt lgkmcnt(0)
	v_mfma_f32_32x32x16_bf16 v[80:95], v[220:223], v[156:159], v[80:95]
	s_add_u32 s44, s44, 0x18000
	s_addc_u32 s45, s45, 0
	s_add_u32 s100, s100, 0x10000
	s_addc_u32 s101, s101, 0
	s_cmp_eq_u32 s44, 0xbe8000
	s_waitcnt vmcnt(0)
	s_waitcnt lgkmcnt(0)
	s_barrier
	s_cbranch_scc1 .LBB0_616

; #define PK4(P, BASE, OUT) do { u32x4 w = {cvtpk(P[BASE + 0], P[BASE + 1]), cvtpk(P[BASE + 2], P[BASE + 3]), cvtpk(P[BASE + 4], P[BASE + 5]), cvtpk(P[BASE + 6], P[BASE + 7])}; \
;     OUT = *reinterpret_cast<bf16x8*>(&w); } while (0)
; __device__ __forceinline__ void smax_tile(f32x16& p0, f32x16& p1, float& mhat, float& l_reg, f32x16 (&o)[4], float* al_l, const bool first, int r32, int hi,
;                                           bf16x8& pa0, bf16x8& pa1, bf16x8& pa2, bf16x8& pa3) {
;     ...
; #pragma unroll
;     for (int r = 0; r < 16; ++r) p0[r] = __builtin_amdgcn_exp2f(p0[r]);
; #pragma unroll
;     for (int r = 0; r < 16; ++r) p1[r] = __builtin_amdgcn_exp2f(p1[r]);
;     float ps = p0[0];
; #pragma unroll
;     for (int r = 1; r < 16; ++r) ps += p0[r];
; #pragma unroll
;     for (int r = 0; r < 16; ++r) ps += p1[r];
;     { auto rr = __builtin_amdgcn_permlane32_swap(__float_as_uint(ps), __float_as_uint(ps), false, false); ps = __uint_as_float(rr[0]) + __uint_as_float(rr[1]); }
;     l_reg += ps;
;     ...
;     PK4(p0, 0, pa0); PK4(p0, 8, pa1); PK4(p1, 0, pa2); PK4(p1, 8, pa3);
.LBB0_651:
	v_exp_f32_e32 v96, v96
	v_exp_f32_e32 v97, v97
	v_exp_f32_e32 v98, v98
	v_exp_f32_e32 v99, v99
	v_exp_f32_e32 v100, v100
	v_exp_f32_e32 v101, v101
	v_add_f32_e32 v128, v96, v97
	v_exp_f32_e32 v102, v102
	v_add_f32_e32 v128, v98, v128
	v_exp_f32_e32 v103, v103
	v_add_f32_e32 v128, v99, v128
	v_exp_f32_e32 v104, v104
	v_add_f32_e32 v128, v100, v128
	v_exp_f32_e32 v105, v105
	v_add_f32_e32 v128, v101, v128
	v_exp_f32_e32 v106, v106
	v_add_f32_e32 v128, v102, v128
	v_exp_f32_e32 v107, v107
	v_add_f32_e32 v128, v103, v128
	v_exp_f32_e32 v108, v108
	v_add_f32_e32 v128, v104, v128
	v_exp_f32_e32 v109, v109
	v_add_f32_e32 v128, v105, v128
	v_exp_f32_e32 v110, v110
	v_add_f32_e32 v128, v106, v128
	v_exp_f32_e32 v111, v111
	v_add_f32_e32 v128, v107, v128
	v_exp_f32_e32 v80, v80
	v_add_f32_e32 v128, v108, v128
	v_exp_f32_e32 v81, v81
	v_add_f32_e32 v128, v109, v128
	v_exp_f32_e32 v82, v82
	v_add_f32_e32 v128, v110, v128
	v_exp_f32_e32 v83, v83
	v_add_f32_e32 v128, v111, v128
	v_exp_f32_e32 v84, v84
	v_add_f32_e32 v128, v80, v128
	v_exp_f32_e32 v85, v85
	v_add_f32_e32 v128, v81, v128
	v_exp_f32_e32 v86, v86
	v_add_f32_e32 v128, v82, v128
	v_exp_f32_e32 v87, v87
	v_add_f32_e32 v128, v83, v128
	v_exp_f32_e32 v88, v88
	v_add_f32_e32 v128, v84, v128
	v_exp_f32_e32 v89, v89
	v_add_f32_e32 v128, v85, v128
	v_exp_f32_e32 v90, v90
	v_add_f32_e32 v128, v86, v128
	v_exp_f32_e32 v91, v91
	v_add_f32_e32 v128, v87, v128
	v_exp_f32_e32 v92, v92
	v_add_f32_e32 v128, v88, v128
	v_exp_f32_e32 v93, v93
	v_add_f32_e32 v128, v89, v128
	v_exp_f32_e32 v94, v94
	v_add_f32_e32 v128, v90, v128
	v_exp_f32_e32 v95, v95
	v_add_f32_e32 v128, v91, v128
	v_add_f32_e32 v128, v92, v128
	v_add_f32_e32 v128, v93, v128
	v_add_f32_e32 v128, v94, v128
	v_add_f32_e32 v128, v95, v128
	v_mov_b32_e32 v129, v128
	v_cvt_pk_bf16_f32 v162, v96, v97
	v_cvt_pk_bf16_f32 v163, v98, v99
	v_permlane32_swap_b32_e32 v128, v129
	v_add_f32_e32 v128, v128, v129
	v_add_f32_e32 v159, v159, v128
	v_cvt_pk_bf16_f32 v164, v100, v101
	v_cvt_pk_bf16_f32 v165, v102, v103
	v_cvt_pk_bf16_f32 v166, v104, v105
	v_cvt_pk_bf16_f32 v167, v106, v107
	v_cvt_pk_bf16_f32 v168, v108, v109
	v_cvt_pk_bf16_f32 v169, v110, v111
	v_cvt_pk_bf16_f32 v132, v80, v81
	v_cvt_pk_bf16_f32 v133, v82, v83
	v_cvt_pk_bf16_f32 v134, v84, v85
	v_cvt_pk_bf16_f32 v135, v86, v87
	v_cvt_pk_bf16_f32 v128, v88, v89
	v_cvt_pk_bf16_f32 v129, v90, v91
	v_cvt_pk_bf16_f32 v130, v92, v93
	v_cvt_pk_bf16_f32 v131, v94, v95
	s_cmp_lg_u32 s86, 0
	s_waitcnt lgkmcnt(0)
	s_barrier
; template <int DQK, bool HASQK, bool HASPV, int J>
; __device__ __forceinline__ void slot_read(bf16x8 (&kf)[DQK / 16][2], s16x4 (&vf)[4][8], const int (&ka_)[4], int vb_) {
;     constexpr int NQS = HASQK ? 2 * (DQK / 16) : 0, NS = NQS + (HASPV ? 16 : 0);
;     if constexpr (J < NQS) { constexpr int d0 = J >> 1, h = J & 1; dsr128<(d0 >> 2) * 128 + h * 32 * DQK * 2>(kf[d0][h], ka_[d0 & 3]); }
;     else if constexpr (J < NS) { constexpr int q = J - NQS, g = q >> 2, d = q & 3; dstr64<v_rd_off(d, g, 0)>(vf[g][2 * d], vb_); dstr64<v_rd_off(d, g, 1)>(vf[g][2 * d + 1], vb_); }
; }
; template <int DQK, bool HASQK, bool HASPV, int J> ...
;     constexpr int NQS = HASQK ? 2 * (DQK / 16) : 0, NS = NQS + (HASPV ? 16 : 0);
;     if constexpr (J < NS) {
;         constexpr int rd1 = (J + 1 < NS) ? ((J + 1 < NQS) ? 1 : 2) : 0, rd2 = (J + 2 < NS) ? ((J + 2 < NQS) ? 1 : 2) : 0, rd3 = (J + 3 < NS) ? ((J + 3 < NQS) ? 1 : 2) : 0, NW = rd1 + rd2 + rd3;
;     ...
;         if constexpr (J < NQS) { constexpr int d0 = J >> 1, h = J & 1;
;             LWN1(kf[d0][h]); SBAR();
;             if constexpr (h == 0) p0 = __builtin_amdgcn_mfma_f32_32x32x16_bf16(kf[d0][0], qr[d0], (d0 == 0) ? negm : p0, 0, 0, 0);
;             else p1 = __builtin_amdgcn_mfma_f32_32x32x16_bf16(kf[d0][1], qr[d0], (d0 == 0) ? negm : p1, 0, 0, 0);
;         } else { constexpr int q = J - NQS, g = q >> 2, d = q & 3;
;             LWN2(vf[g][2 * d], vf[g][2 * d + 1]); SBAR();
;             o[d] = __builtin_amdgcn_mfma_f32_32x32x16_bf16(pa[g], (bf16x8){vf[g][2 * d][0], vf[g][2 * d][1], vf[g][2 * d][2], vf[g][2 * d][3], vf[g][2 * d + 1][0], vf[g][2 * d + 1][1], vf[g][2 * d + 1][2], vf[g][2 * d + 1][3]}, o[d], 0, 0, 0);
;         }
;     ...
;         SBAR();
;         slot_read<DQK, HASQK, HASPV, J + 4>(kf, vf, ka_, vb_);
;         SBAR();
;         slot_run<DQK, HASQK, HASPV, J + 1>(kf, vf, ka_, vb_, qr, p0, p1, negm, o, pa);
;     }
; }
;     ...
;     for (int i = 0; i < NT - 1; ++i) {
;         SEG_S(i);
;         { const int cp = (ci == 0) ? 2 : ci - 1, cn = (ci == 2) ? 0 : ci + 1;
;           if (DMA_M) { if (i + 3 < NT) DMA_K(i + 3, cp); if (i + 2 < NT) DMA_V(i + 2, cn); }
;           SEG_M(true, true, ci, cp);
;           if (DMA_M && i + 3 < NT) asm volatile("s_waitcnt vmcnt(%0)" :: "n"(NKW + 2) : "memory");
;           else asm volatile("s_waitcnt vmcnt(0)" ::: "memory");
;           BAR_ALL(); }
	s_cselect_b32 s46, s87, 0x8000
	s_lshl_b32 s47, s86, 13
	v_add_u32_e32 v81, s47, v141
	v_add_u32_e32 v82, s47, v143
	ds_read_b128 v[170:173], v81 offset:0
	ds_read_b128 v[174:177], v81 offset:0x1000
	ds_read_b128 v[178:181], v82 offset:0
	ds_read_b128 v[182:185], v82 offset:0x1000
	v_xor_b32_e32 v80, 0x80000000, v158
	v_add_u32_e32 v186, s47, v160
	v_add_u32_e32 v187, s47, v161
	v_add_u32_e32 v188, s46, v157
	v_mov_b32_e32 v81, v80
	v_mov_b32_e32 v82, v80
	v_mov_b32_e32 v83, v80
	v_mov_b32_e32 v84, v80
	v_mov_b32_e32 v85, v80
	v_mov_b32_e32 v86, v80
	v_mov_b32_e32 v87, v80
	v_mov_b32_e32 v88, v80
	v_mov_b32_e32 v89, v80
	v_mov_b32_e32 v90, v80
	v_mov_b32_e32 v91, v80
	v_mov_b32_e32 v92, v80
	v_mov_b32_e32 v93, v80
	v_mov_b32_e32 v94, v80
	v_mov_b32_e32 v95, v80
	s_waitcnt lgkmcnt(3)
	s_nop 1
	v_mfma_f32_32x32x16_bf16 v[96:111], v[170:173], v[112:115], v[80:95]
	ds_read_b128 v[170:173], v186 offset:0
	s_waitcnt lgkmcnt(3)
	s_nop 0
	v_mfma_f32_32x32x16_bf16 v[80:95], v[174:177], v[112:115], v[80:95]
	ds_read_b128 v[174:177], v186 offset:0x1000
	s_waitcnt lgkmcnt(3)
	s_nop 0
	v_mfma_f32_32x32x16_bf16 v[96:111], v[178:181], v[116:119], v[96:111]
	ds_read_b128 v[178:181], v187 offset:0
	s_waitcnt lgkmcnt(3)
	s_nop 0
	v_mfma_f32_32x32x16_bf16 v[80:95], v[182:185], v[116:119], v[80:95]
	ds_read_b128 v[182:185], v187 offset:0x1000
	s_waitcnt lgkmcnt(3)
	s_nop 0
	v_mfma_f32_32x32x16_bf16 v[96:111], v[170:173], v[120:123], v[96:111]
	ds_read_b64_tr_b16 v[170:171], v188 offset:0
	ds_read_b64_tr_b16 v[172:173], v188 offset:0x800
	s_waitcnt lgkmcnt(4)
	s_nop 0
	v_mfma_f32_32x32x16_bf16 v[80:95], v[174:177], v[120:123], v[80:95]
	ds_read_b64_tr_b16 v[174:175], v188 offset:0x200
	ds_read_b64_tr_b16 v[176:177], v188 offset:0xa00
	s_waitcnt lgkmcnt(5)
	s_nop 0
	v_mfma_f32_32x32x16_bf16 v[96:111], v[178:181], v[124:127], v[96:111]
	ds_read_b64_tr_b16 v[178:179], v188 offset:0x400
	ds_read_b64_tr_b16 v[180:181], v188 offset:0xc00
	s_waitcnt lgkmcnt(6)
	s_nop 0
	v_mfma_f32_32x32x16_bf16 v[80:95], v[182:185], v[124:127], v[80:95]
	ds_read_b64_tr_b16 v[182:183], v188 offset:0x600
	ds_read_b64_tr_b16 v[184:185], v188 offset:0xe00
	s_waitcnt lgkmcnt(6)
	s_nop 0
	v_mfma_f32_32x32x16_bf16 v[64:79], v[162:165], v[170:173], v[64:79]
	ds_read_b64_tr_b16 v[170:171], v188 offset:0x1000
	ds_read_b64_tr_b16 v[172:173], v188 offset:0x1800
	s_waitcnt lgkmcnt(6)
	s_nop 0
	v_mfma_f32_32x32x16_bf16 v[48:63], v[162:165], v[174:177], v[48:63]
	ds_read_b64_tr_b16 v[174:175], v188 offset:0x1200
	ds_read_b64_tr_b16 v[176:177], v188 offset:0x1a00
	s_waitcnt lgkmcnt(6)
	s_nop 0
	v_mfma_f32_32x32x16_bf16 v[32:47], v[162:165], v[178:181], v[32:47]
	ds_read_b64_tr_b16 v[178:179], v188 offset:0x1400
	ds_read_b64_tr_b16 v[180:181], v188 offset:0x1c00
	s_waitcnt lgkmcnt(6)
	s_nop 0
	v_mfma_f32_32x32x16_bf16 v[16:31], v[162:165], v[182:185], v[16:31]
	ds_read_b64_tr_b16 v[162:163], v188 offset:0x1600
	ds_read_b64_tr_b16 v[164:165], v188 offset:0x1e00
	s_waitcnt lgkmcnt(6)
	s_nop 0
	v_mfma_f32_32x32x16_bf16 v[64:79], v[166:169], v[170:173], v[64:79]
	ds_read_b64_tr_b16 v[170:171], v188 offset:0x2000
	ds_read_b64_tr_b16 v[172:173], v188 offset:0x2800
	s_waitcnt lgkmcnt(6)
	s_nop 0
	v_mfma_f32_32x32x16_bf16 v[48:63], v[166:169], v[174:177], v[48:63]
	ds_read_b64_tr_b16 v[174:175], v188 offset:0x2200
	ds_read_b64_tr_b16 v[176:177], v188 offset:0x2a00
	s_waitcnt lgkmcnt(6)
	s_nop 0
	v_mfma_f32_32x32x16_bf16 v[32:47], v[166:169], v[178:181], v[32:47]
	ds_read_b64_tr_b16 v[178:179], v188 offset:0x2400
	ds_read_b64_tr_b16 v[180:181], v188 offset:0x2c00
	s_waitcnt lgkmcnt(6)
	s_nop 0
	v_mfma_f32_32x32x16_bf16 v[16:31], v[166:169], v[162:165], v[16:31]
	ds_read_b64_tr_b16 v[162:163], v188 offset:0x2600
	ds_read_b64_tr_b16 v[164:165], v188 offset:0x2e00
	s_waitcnt lgkmcnt(6)
	s_nop 0
	v_mfma_f32_32x32x16_bf16 v[64:79], v[132:135], v[170:173], v[64:79]
	ds_read_b64_tr_b16 v[166:167], v188 offset:0x3000
	ds_read_b64_tr_b16 v[168:169], v188 offset:0x3800
	s_waitcnt lgkmcnt(6)
	s_nop 0
	v_mfma_f32_32x32x16_bf16 v[48:63], v[132:135], v[174:177], v[48:63]
	ds_read_b64_tr_b16 v[170:171], v188 offset:0x3200
	ds_read_b64_tr_b16 v[172:173], v188 offset:0x3a00
	s_waitcnt lgkmcnt(6)
	s_nop 0
	v_mfma_f32_32x32x16_bf16 v[32:47], v[132:135], v[178:181], v[32:47]
	ds_read_b64_tr_b16 v[174:175], v188 offset:0x3400
	ds_read_b64_tr_b16 v[176:177], v188 offset:0x3c00
	s_waitcnt lgkmcnt(6)
	s_nop 0
	v_mfma_f32_32x32x16_bf16 v[16:31], v[132:135], v[162:165], v[16:31]
	ds_read_b64_tr_b16 v[132:133], v188 offset:0x3600
	ds_read_b64_tr_b16 v[134:135], v188 offset:0x3e00
	s_waitcnt lgkmcnt(6)
	s_nop 0
	v_mfma_f32_32x32x16_bf16 v[64:79], v[128:131], v[166:169], v[64:79]
	s_waitcnt lgkmcnt(4)
	s_nop 0
	v_mfma_f32_32x32x16_bf16 v[48:63], v[128:131], v[170:173], v[48:63]
	s_waitcnt lgkmcnt(2)
	s_nop 0
	v_mfma_f32_32x32x16_bf16 v[32:47], v[128:131], v[174:177], v[32:47]
	s_waitcnt lgkmcnt(0)
	s_nop 0
	v_mfma_f32_32x32x16_bf16 v[16:31], v[128:131], v[132:135], v[16:31]
	s_add_u32 s98, s98, 0x10000
	s_addc_u32 s99, s99, 0
	s_add_u32 s100, s100, 0x10000
	s_addc_u32 s101, s101, 0
	s_waitcnt vmcnt(0)
	s_add_u32 s44, s44, 0x10000
	s_addc_u32 s45, s45, 0
	s_cmp_eq_u32 s44, 0x7f0000
	s_waitcnt lgkmcnt(0)
	s_barrier
	s_cbranch_scc1 .LBB0_662
